# v82 plus merge-epilogue: the gate bytes of rounds 2-4 are prefetched (loads into dead registers) together with round 1's loads
# baseline (speedup 1.0000x reference)
.LBB0_874:
	s_mov_b64 s[98:99], 0x1000
	v_lshl_add_u64 v[182:183], v[148:149], 0, s[92:93]
	global_load_dwordx2 v[184:185], v[182:183], off offset:2048
	global_load_dwordx2 v[186:187], v[182:183], off offset:2560
	global_load_dwordx2 v[188:189], v[182:183], off offset:3072
	global_load_dwordx2 v[190:191], v[182:183], off offset:3584
	v_lshl_add_u64 v[182:183], v[182:183], 0, s[98:99]
	global_load_dwordx2 v[192:193], v[182:183], off
	global_load_dwordx2 v[194:195], v[182:183], off offset:512
	global_load_dwordx2 v[196:197], v[182:183], off offset:1024
	global_load_dwordx2 v[198:199], v[182:183], off offset:1536
	global_load_dwordx2 v[200:201], v[182:183], off offset:2048
	global_load_dwordx2 v[202:203], v[182:183], off offset:2560
	global_load_dwordx2 v[204:205], v[182:183], off offset:3072
	global_load_dwordx2 v[206:207], v[182:183], off offset:3584
	s_and_b64 vcc, exec, s[22:23]
	s_cbranch_vccz .Ltpf_done
	v_lshl_add_u64 v[182:183], v[148:149], 0, s[90:91]
	global_load_dwordx2 v[208:209], v[182:183], off offset:2048
	global_load_dwordx2 v[210:211], v[182:183], off offset:2560
	global_load_dwordx2 v[184:185], v[182:183], off offset:3072
	global_load_dwordx2 v[186:187], v[182:183], off offset:3584
	v_lshl_add_u64 v[182:183], v[182:183], 0, s[98:99]
	global_load_dwordx2 v[188:189], v[182:183], off
	global_load_dwordx2 v[190:191], v[182:183], off offset:512
	global_load_dwordx2 v[192:193], v[182:183], off offset:1024
	global_load_dwordx2 v[194:195], v[182:183], off offset:1536
	global_load_dwordx2 v[196:197], v[182:183], off offset:2048
	global_load_dwordx2 v[198:199], v[182:183], off offset:2560
	global_load_dwordx2 v[200:201], v[182:183], off offset:3072
	global_load_dwordx2 v[202:203], v[182:183], off offset:3584
